# v22 plus first-iteration load-segment waits of P1/P4/P11 counted past the previous unit's epilogue stores (vmcnt 8 -> 8+stores)
# baseline (speedup 1.0000x reference)
.LBB0_260:
	s_ashr_i32 s41, s40, 31
	s_lshl_b64 s[42:43], s[40:41], 19
	s_add_u32 s42, s54, s42
	s_addc_u32 s43, s55, s43
	s_and_b64 s[44:45], s[4:5], exec
	ds_read_b128 v[0:3], v219
	ds_read_b128 v[4:7], v219 offset:1024
	ds_read_b128 v[8:11], v219 offset:2048
	ds_read_b128 v[12:15], v219 offset:3072
	ds_read_b128 v[16:19], v220
	ds_read_b128 v[20:23], v220 offset:1024
	ds_read_b128 v[24:27], v220 offset:2048
	ds_read_b128 v[28:31], v220 offset:3072
	s_cselect_b32 s7, s43, s13
	s_cselect_b32 s11, s42, s12
	s_ashr_i32 s39, s38, 31
	s_lshl_b64 s[44:45], s[38:39], 19
	s_add_u32 s44, s56, s44
	s_addc_u32 s45, s57, s45
	s_and_b64 s[46:47], s[4:5], exec
	s_cselect_b32 s39, s45, s9
	s_cselect_b32 s41, s44, s8
	s_add_u32 s46, s12, 0x100
	s_addc_u32 s47, s13, 0
	s_add_u32 s52, s8, 0x100
	s_addc_u32 s53, s9, 0
	s_add_u32 s48, s12, 0x180
	s_addc_u32 s49, s13, 0
	ds_read_b128 v[32:35], v221
	ds_read_b128 v[36:39], v221 offset:1024
	ds_read_b128 v[40:43], v221 offset:2048
	ds_read_b128 v[44:47], v221 offset:3072
	ds_read_b128 v[48:51], v221 offset:4096
	ds_read_b128 v[52:55], v221 offset:5120
	ds_read_b128 v[56:59], v221 offset:6144
	ds_read_b128 v[60:63], v221 offset:7168
	s_add_u32 s50, s8, 0x180
	s_addc_u32 s51, s9, 0
	s_add_u32 s76, s12, 0x40080
	s_addc_u32 s77, s13, 0
	s_add_i32 m0, s59, 0xc000
	s_nop 0
	global_load_lds_dwordx4 v215, s[76:77]
	s_nop 0
	s_add_i32 m0, s59, 0xe000
	s_nop 0
	global_load_lds_dwordx4 v217, s[76:77]
	s_waitcnt vmcnt(24) lgkmcnt(0)
	s_barrier
	s_waitcnt lgkmcnt(7)
	v_mfma_i32_16x16x64_i8 v[64:67], v[0:3], v[32:35], 0
	s_mov_b32 s76, 0
	v_mfma_i32_16x16x64_i8 v[68:71], v[8:11], v[32:35], 0
	s_waitcnt lgkmcnt(5)
	v_mfma_i32_16x16x64_i8 v[72:75], v[0:3], v[40:43], 0
	v_mfma_i32_16x16x64_i8 v[76:79], v[8:11], v[40:43], 0
	s_waitcnt lgkmcnt(3)
	v_mfma_i32_16x16x64_i8 v[84:87], v[8:11], v[48:51], 0
	s_waitcnt lgkmcnt(1)
	v_mfma_i32_16x16x64_i8 v[88:91], v[0:3], v[56:59], 0
	v_mfma_i32_16x16x64_i8 v[140:143], v[4:7], v[36:39], v[64:67]
	v_mfma_i32_16x16x64_i8 v[144:147], v[12:15], v[36:39], v[68:71]
	v_mfma_i32_16x16x64_i8 v[152:155], v[4:7], v[44:47], v[72:75]
	v_mfma_i32_16x16x64_i8 v[156:159], v[12:15], v[44:47], v[76:79]
	v_mfma_i32_16x16x64_i8 v[80:83], v[0:3], v[48:51], 0
	v_mfma_i32_16x16x64_i8 v[84:87], v[12:15], v[52:55], v[84:87]
	s_waitcnt lgkmcnt(0)
	v_mfma_i32_16x16x64_i8 v[88:91], v[4:7], v[60:63], v[88:91]
	v_mfma_i32_16x16x64_i8 v[92:95], v[8:11], v[56:59], 0
	v_mfma_i32_16x16x64_i8 v[80:83], v[4:7], v[52:55], v[80:83]
	v_mfma_i32_16x16x64_i8 v[92:95], v[12:15], v[60:63], v[92:95]
	v_mfma_i32_16x16x64_i8 v[96:99], v[16:19], v[32:35], 0
	v_mfma_i32_16x16x64_i8 v[32:35], v[24:27], v[32:35], 0
	v_mfma_i32_16x16x64_i8 v[96:99], v[20:23], v[36:39], v[96:99]
	v_mfma_i32_16x16x64_i8 v[32:35], v[28:31], v[36:39], v[32:35]
	v_mfma_i32_16x16x64_i8 v[36:39], v[16:19], v[40:43], 0
	v_mfma_i32_16x16x64_i8 v[40:43], v[24:27], v[40:43], 0
	v_mfma_i32_16x16x64_i8 v[36:39], v[20:23], v[44:47], v[36:39]
	v_mfma_i32_16x16x64_i8 v[40:43], v[28:31], v[44:47], v[40:43]
	v_mfma_i32_16x16x64_i8 v[44:47], v[16:19], v[48:51], 0
	v_mfma_i32_16x16x64_i8 v[48:51], v[24:27], v[48:51], 0
	v_mfma_i32_16x16x64_i8 v[44:47], v[20:23], v[52:55], v[44:47]
	v_mfma_i32_16x16x64_i8 v[48:51], v[28:31], v[52:55], v[48:51]
	v_mfma_i32_16x16x64_i8 v[52:55], v[16:19], v[56:59], 0
	v_mfma_i32_16x16x64_i8 v[56:59], v[24:27], v[56:59], 0
	v_mfma_i32_16x16x64_i8 v[52:55], v[20:23], v[60:63], v[52:55]
	v_mfma_i32_16x16x64_i8 v[56:59], v[28:31], v[60:63], v[56:59]
	s_barrier
	ds_read_b128 v[60:63], v221 offset:16384
	ds_read_b128 v[100:103], v221 offset:17408
	ds_read_b128 v[104:107], v221 offset:18432
	ds_read_b128 v[108:111], v221 offset:19456
	ds_read_b128 v[112:115], v221 offset:20480
	ds_read_b128 v[116:119], v221 offset:21504
	ds_read_b128 v[120:123], v221 offset:22528
	ds_read_b128 v[124:127], v221 offset:23552
	s_add_i32 m0, s59, 0x10000
	s_nop 0
	global_load_lds_dwordx4 v216, s[52:53]
	s_nop 0
	s_add_i32 m0, s59, 0x12000
	s_nop 0
	global_load_lds_dwordx4 v218, s[52:53]
	s_add_u32 s52, s8, 0x40100
	s_addc_u32 s53, s9, 0
	s_add_i32 m0, s59, 0x14000
	s_nop 0
	global_load_lds_dwordx4 v216, s[52:53]
	s_nop 0
	s_add_i32 m0, s59, 0x16000
	s_nop 0
	global_load_lds_dwordx4 v218, s[52:53]
	s_nop 0
	s_add_i32 m0, s59, 0
	s_nop 0
	global_load_lds_dwordx4 v215, s[46:47]
	s_nop 0
	s_add_i32 m0, s59, 0x2000
	s_nop 0
	global_load_lds_dwordx4 v217, s[46:47]
	s_waitcnt vmcnt(24) lgkmcnt(0)
	s_barrier
	v_mfma_i32_16x16x64_i8 v[136:139], v[0:3], v[104:107], 0
	v_mfma_i32_16x16x64_i8 v[228:231], v[4:7], v[108:111], v[136:139]
	v_mfma_i32_16x16x64_i8 v[136:139], v[8:11], v[104:107], 0
	v_mfma_i32_16x16x64_i8 v[128:131], v[0:3], v[60:63], 0
	v_mfma_i32_16x16x64_i8 v[132:135], v[8:11], v[60:63], 0
	v_mfma_i32_16x16x64_i8 v[232:235], v[12:15], v[108:111], v[136:139]
	v_mfma_i32_16x16x64_i8 v[136:139], v[0:3], v[112:115], 0
	v_mfma_i32_16x16x64_i8 v[0:3], v[0:3], v[120:123], 0
	v_mfma_i32_16x16x64_i8 v[128:131], v[4:7], v[100:103], v[128:131]
	v_mfma_i32_16x16x64_i8 v[132:135], v[12:15], v[100:103], v[132:135]
	v_mfma_i32_16x16x64_i8 v[236:239], v[4:7], v[116:119], v[136:139]
	v_mfma_i32_16x16x64_i8 v[136:139], v[8:11], v[112:115], 0
	v_mfma_i32_16x16x64_i8 v[0:3], v[4:7], v[124:127], v[0:3]
	v_mfma_i32_16x16x64_i8 v[4:7], v[8:11], v[120:123], 0
	v_mfma_i32_16x16x64_i8 v[240:243], v[12:15], v[116:119], v[136:139]
	v_mfma_i32_16x16x64_i8 v[4:7], v[12:15], v[124:127], v[4:7]
	v_mfma_i32_16x16x64_i8 v[8:11], v[16:19], v[60:63], 0
	v_mfma_i32_16x16x64_i8 v[12:15], v[24:27], v[60:63], 0
	v_mfma_i32_16x16x64_i8 v[8:11], v[20:23], v[100:103], v[8:11]
	v_mfma_i32_16x16x64_i8 v[12:15], v[28:31], v[100:103], v[12:15]
	v_mfma_i32_16x16x64_i8 v[60:63], v[16:19], v[104:107], 0
	v_mfma_i32_16x16x64_i8 v[100:103], v[24:27], v[104:107], 0
	v_mfma_i32_16x16x64_i8 v[104:107], v[16:19], v[112:115], 0
	v_mfma_i32_16x16x64_i8 v[16:19], v[16:19], v[120:123], 0
	v_mfma_i32_16x16x64_i8 v[60:63], v[20:23], v[108:111], v[60:63]
	v_mfma_i32_16x16x64_i8 v[100:103], v[28:31], v[108:111], v[100:103]
	v_mfma_i32_16x16x64_i8 v[244:247], v[20:23], v[116:119], v[104:107]
	v_mfma_i32_16x16x64_i8 v[104:107], v[24:27], v[112:115], 0
	v_mfma_i32_16x16x64_i8 v[16:19], v[20:23], v[124:127], v[16:19]
	v_mfma_i32_16x16x64_i8 v[20:23], v[24:27], v[120:123], 0
	v_mfma_i32_16x16x64_i8 v[248:251], v[28:31], v[116:119], v[104:107]
	v_mfma_i32_16x16x64_i8 v[20:23], v[28:31], v[124:127], v[20:23]
	s_barrier
	ds_read_b128 v[24:27], v222
	ds_read_b128 v[28:31], v222 offset:1024
	ds_read_b128 v[112:115], v222 offset:2048
	ds_read_b128 v[116:119], v222 offset:3072
	ds_read_b128 v[208:211], v223
	ds_read_b128 v[224:227], v223 offset:1024
	ds_read_b128 v[64:67], v223 offset:2048
	ds_read_b128 v[68:71], v223 offset:3072
	ds_read_b128 v[104:107], v221 offset:32768
	ds_read_b128 v[108:111], v221 offset:33792
	ds_read_b128 v[120:123], v221 offset:34816
	ds_read_b128 v[124:127], v221 offset:35840
	ds_read_b128 v[136:139], v221 offset:36864
	ds_read_b128 v[148:151], v221 offset:37888
	ds_read_b128 v[72:75], v221 offset:38912
	ds_read_b128 v[76:79], v221 offset:39936
	s_add_u32 s12, s12, 0x40100
	s_addc_u32 s13, s13, 0
	s_add_i32 m0, s59, 0x4000
	s_nop 0
	global_load_lds_dwordx4 v215, s[12:13]
	s_nop 0
	s_add_i32 m0, s59, 0x6000
	s_nop 0
	global_load_lds_dwordx4 v217, s[12:13]
	s_waitcnt vmcnt(8) lgkmcnt(0)
	s_barrier
	v_mfma_i32_16x16x64_i8 v[140:143], v[24:27], v[104:107], v[140:143]
	v_mfma_i32_16x16x64_i8 v[80:83], v[24:27], v[136:139], v[80:83]
	v_mfma_i32_16x16x64_i8 v[204:207], v[28:31], v[108:111], v[140:143]
	v_mfma_i32_16x16x64_i8 v[140:143], v[112:115], v[104:107], v[144:147]
	v_mfma_i32_16x16x64_i8 v[172:175], v[28:31], v[148:151], v[80:83]
	v_mfma_i32_16x16x64_i8 v[80:83], v[112:115], v[136:139], v[84:87]
	v_mfma_i32_16x16x64_i8 v[200:203], v[116:119], v[108:111], v[140:143]
	v_mfma_i32_16x16x64_i8 v[140:143], v[24:27], v[120:123], v[152:155]
	v_mfma_i32_16x16x64_i8 v[168:171], v[116:119], v[148:151], v[80:83]
	v_mfma_i32_16x16x64_i8 v[80:83], v[24:27], v[72:75], v[88:91]
	v_mfma_i32_16x16x64_i8 v[188:191], v[28:31], v[124:127], v[140:143]
	v_mfma_i32_16x16x64_i8 v[140:143], v[112:115], v[120:123], v[156:159]
	v_mfma_i32_16x16x64_i8 v[156:159], v[28:31], v[76:79], v[80:83]
	v_mfma_i32_16x16x64_i8 v[80:83], v[112:115], v[72:75], v[92:95]
	v_mfma_i32_16x16x64_i8 v[184:187], v[116:119], v[124:127], v[140:143]
	v_mfma_i32_16x16x64_i8 v[152:155], v[116:119], v[76:79], v[80:83]
	v_mfma_i32_16x16x64_i8 v[32:35], v[64:67], v[104:107], v[32:35]
	v_mfma_i32_16x16x64_i8 v[192:195], v[68:71], v[108:111], v[32:35]
	v_mfma_i32_16x16x64_i8 v[32:35], v[208:211], v[120:123], v[36:39]
	v_mfma_i32_16x16x64_i8 v[180:183], v[224:227], v[124:127], v[32:35]
	v_mfma_i32_16x16x64_i8 v[32:35], v[64:67], v[120:123], v[40:43]
	v_mfma_i32_16x16x64_i8 v[176:179], v[68:71], v[124:127], v[32:35]
	v_mfma_i32_16x16x64_i8 v[32:35], v[208:211], v[136:139], v[44:47]
	v_mfma_i32_16x16x64_i8 v[164:167], v[224:227], v[148:151], v[32:35]
	v_mfma_i32_16x16x64_i8 v[32:35], v[64:67], v[136:139], v[48:51]
	v_mfma_i32_16x16x64_i8 v[160:163], v[68:71], v[148:151], v[32:35]
	v_mfma_i32_16x16x64_i8 v[32:35], v[208:211], v[72:75], v[52:55]
	v_mfma_i32_16x16x64_i8 v[80:83], v[208:211], v[104:107], v[96:99]
	v_mfma_i32_16x16x64_i8 v[148:151], v[224:227], v[76:79], v[32:35]
	v_mfma_i32_16x16x64_i8 v[32:35], v[64:67], v[72:75], v[56:59]
	v_mfma_i32_16x16x64_i8 v[196:199], v[224:227], v[108:111], v[80:83]
	v_mfma_i32_16x16x64_i8 v[144:147], v[68:71], v[76:79], v[32:35]
	s_barrier
	s_nop 3
	ds_read_b128 v[32:35], v221 offset:49152
	ds_read_b128 v[36:39], v221 offset:50176
	ds_read_b128 v[40:43], v221 offset:51200
	ds_read_b128 v[44:47], v221 offset:52224
	ds_read_b128 v[48:51], v221 offset:53248
	ds_read_b128 v[52:55], v221 offset:54272
	ds_read_b128 v[56:59], v221 offset:55296
	ds_read_b128 v[76:79], v221 offset:56320
	s_add_i32 m0, s59, 0x18000
	s_nop 0
	global_load_lds_dwordx4 v216, s[50:51]
	s_nop 0
	s_add_i32 m0, s59, 0x1a000
	s_nop 0
	global_load_lds_dwordx4 v218, s[50:51]
	s_add_u32 s12, s8, 0x40180
	s_addc_u32 s13, s9, 0
	s_add_i32 m0, s59, 0x1c000
	s_nop 0
	global_load_lds_dwordx4 v216, s[12:13]
	s_nop 0
	s_add_i32 m0, s59, 0x1e000
	s_nop 0
	global_load_lds_dwordx4 v218, s[12:13]
	s_nop 0
	s_add_i32 m0, s59, 0x8000
	s_nop 0
	global_load_lds_dwordx4 v215, s[48:49]
	s_nop 0
	s_add_i32 m0, s59, 0xa000
	s_nop 0
	global_load_lds_dwordx4 v217, s[48:49]
	s_waitcnt vmcnt(8) lgkmcnt(0)
	s_barrier
	v_mfma_i32_16x16x64_i8 v[72:75], v[24:27], v[32:35], v[128:131]
	v_mfma_i32_16x16x64_i8 v[140:143], v[28:31], v[36:39], v[72:75]
	v_mfma_i32_16x16x64_i8 v[72:75], v[112:115], v[32:35], v[132:135]
	v_mfma_i32_16x16x64_i8 v[136:139], v[116:119], v[36:39], v[72:75]
	v_mfma_i32_16x16x64_i8 v[72:75], v[24:27], v[40:43], v[228:231]
	v_mfma_i32_16x16x64_i8 v[124:127], v[28:31], v[44:47], v[72:75]
	v_mfma_i32_16x16x64_i8 v[72:75], v[112:115], v[40:43], v[232:235]
	v_mfma_i32_16x16x64_i8 v[120:123], v[116:119], v[44:47], v[72:75]
	v_mfma_i32_16x16x64_i8 v[72:75], v[24:27], v[48:51], v[236:239]
	v_mfma_i32_16x16x64_i8 v[0:3], v[24:27], v[56:59], v[0:3]
	v_mfma_i32_16x16x64_i8 v[108:111], v[28:31], v[52:55], v[72:75]
	v_mfma_i32_16x16x64_i8 v[72:75], v[112:115], v[48:51], v[240:243]
	v_mfma_i32_16x16x64_i8 v[88:91], v[28:31], v[76:79], v[0:3]
	v_mfma_i32_16x16x64_i8 v[0:3], v[112:115], v[56:59], v[4:7]
	v_mfma_i32_16x16x64_i8 v[104:107], v[116:119], v[52:55], v[72:75]
	v_mfma_i32_16x16x64_i8 v[84:87], v[116:119], v[76:79], v[0:3]
	v_mfma_i32_16x16x64_i8 v[0:3], v[208:211], v[32:35], v[8:11]
	v_mfma_i32_16x16x64_i8 v[132:135], v[224:227], v[36:39], v[0:3]
	v_mfma_i32_16x16x64_i8 v[0:3], v[64:67], v[32:35], v[12:15]
	v_mfma_i32_16x16x64_i8 v[128:131], v[68:71], v[36:39], v[0:3]
	v_mfma_i32_16x16x64_i8 v[0:3], v[208:211], v[40:43], v[60:63]
	v_mfma_i32_16x16x64_i8 v[116:119], v[224:227], v[44:47], v[0:3]
	v_mfma_i32_16x16x64_i8 v[0:3], v[64:67], v[40:43], v[100:103]
	v_mfma_i32_16x16x64_i8 v[112:115], v[68:71], v[44:47], v[0:3]
	v_mfma_i32_16x16x64_i8 v[0:3], v[208:211], v[48:51], v[244:247]
	v_mfma_i32_16x16x64_i8 v[100:103], v[224:227], v[52:55], v[0:3]
	v_mfma_i32_16x16x64_i8 v[0:3], v[64:67], v[48:51], v[248:251]
	v_mfma_i32_16x16x64_i8 v[96:99], v[68:71], v[52:55], v[0:3]
	v_mfma_i32_16x16x64_i8 v[0:3], v[208:211], v[56:59], v[16:19]
	v_mfma_i32_16x16x64_i8 v[72:75], v[224:227], v[76:79], v[0:3]
	v_mfma_i32_16x16x64_i8 v[0:3], v[64:67], v[56:59], v[20:23]
	v_mfma_i32_16x16x64_i8 v[68:71], v[68:71], v[76:79], v[0:3]
	s_barrier
	s_add_u32 s77, s8, 0x200
	s_addc_u32 s80, s9, 0

.LBB0_752:
	s_ashr_i32 s17, s16, 31
	s_lshl_b64 s[18:19], s[16:17], 19
	s_add_u32 s18, s40, s18
	s_addc_u32 s19, s41, s19
	s_and_b64 s[20:21], s[4:5], exec
	s_cselect_b32 s58, s19, s29
	s_cselect_b32 s59, s18, s28
	s_ashr_i32 s15, s14, 31
	s_lshl_b64 s[20:21], s[14:15], 19
	s_add_u32 s20, s42, s20
	s_addc_u32 s21, s43, s21
	s_and_b64 s[26:27], s[4:5], exec
	ds_read_b128 v[0:3], v204 offset:3072
	ds_read_b128 v[4:7], v204 offset:2048
	ds_read_b128 v[8:11], v204 offset:1024
	ds_read_b128 v[12:15], v204
	ds_read_b128 v[16:19], v205 offset:3072
	ds_read_b128 v[20:23], v205 offset:2048
	ds_read_b128 v[24:27], v205 offset:1024
	ds_read_b128 v[28:31], v205
	ds_read_b128 v[32:35], v206
	ds_read_b128 v[36:39], v206 offset:1024
	ds_read_b128 v[40:43], v206 offset:2048
	ds_read_b128 v[44:47], v206 offset:3072
	ds_read_b128 v[48:51], v206 offset:4096
	ds_read_b128 v[52:55], v206 offset:5120
	ds_read_b128 v[56:59], v206 offset:6144
	ds_read_b128 v[60:63], v206 offset:7168
	s_cselect_b32 s15, s21, s25
	s_cselect_b32 s60, s20, s24
	s_lshl_b32 s26, s55, 11
	s_and_b32 s26, s26, 0x800
	s_or_b32 s38, s26, s49
	s_lshl_b64 s[30:31], s[16:17], 11
	s_add_u32 s26, s28, 0x100
	s_addc_u32 s27, s29, 0
	s_add_u32 s62, s24, 0x100
	s_addc_u32 s63, s25, 0
	s_add_u32 s34, s28, 0x180
	s_addc_u32 s35, s29, 0
	s_add_u32 s36, s24, 0x180
	s_addc_u32 s37, s25, 0
	s_add_u32 s66, s28, 0x40080
	s_addc_u32 s67, s29, 0
	s_add_i32 m0, s46, 0xc000
	s_nop 0
	global_load_lds_dwordx4 v199, s[66:67]
	s_nop 0
	s_add_i32 m0, s46, 0xe000
	s_nop 0
	global_load_lds_dwordx4 v201, s[66:67]
	s_waitcnt vmcnt(16) lgkmcnt(0)
	s_barrier
	s_waitcnt lgkmcnt(7)
	v_mfma_i32_16x16x64_i8 v[64:67], v[28:31], v[32:35], 0
	s_mov_b32 s17, 0
	v_mfma_i32_16x16x64_i8 v[68:71], v[20:23], v[32:35], 0
	s_waitcnt lgkmcnt(5)
	v_mfma_i32_16x16x64_i8 v[72:75], v[28:31], v[40:43], 0
	v_mfma_i32_16x16x64_i8 v[132:135], v[24:27], v[36:39], v[64:67]
	v_mfma_i32_16x16x64_i8 v[136:139], v[16:19], v[36:39], v[68:71]
	s_waitcnt lgkmcnt(4)
	v_mfma_i32_16x16x64_i8 v[144:147], v[24:27], v[44:47], v[72:75]
	v_mfma_i32_16x16x64_i8 v[76:79], v[20:23], v[40:43], 0
	s_waitcnt lgkmcnt(3)
	v_mfma_i32_16x16x64_i8 v[80:83], v[28:31], v[48:51], 0
	v_mfma_i32_16x16x64_i8 v[84:87], v[20:23], v[48:51], 0
	s_waitcnt lgkmcnt(1)
	v_mfma_i32_16x16x64_i8 v[88:91], v[28:31], v[56:59], 0
	v_mfma_i32_16x16x64_i8 v[92:95], v[20:23], v[56:59], 0
	v_mfma_i32_16x16x64_i8 v[76:79], v[16:19], v[44:47], v[76:79]
	v_mfma_i32_16x16x64_i8 v[80:83], v[24:27], v[52:55], v[80:83]
	v_mfma_i32_16x16x64_i8 v[84:87], v[16:19], v[52:55], v[84:87]
	s_waitcnt lgkmcnt(0)
	v_mfma_i32_16x16x64_i8 v[88:91], v[24:27], v[60:63], v[88:91]
	v_mfma_i32_16x16x64_i8 v[92:95], v[16:19], v[60:63], v[92:95]
	v_mfma_i32_16x16x64_i8 v[96:99], v[12:15], v[32:35], 0
	v_mfma_i32_16x16x64_i8 v[32:35], v[4:7], v[32:35], 0
	v_mfma_i32_16x16x64_i8 v[96:99], v[8:11], v[36:39], v[96:99]
	v_mfma_i32_16x16x64_i8 v[32:35], v[0:3], v[36:39], v[32:35]
	v_mfma_i32_16x16x64_i8 v[36:39], v[12:15], v[40:43], 0
	v_mfma_i32_16x16x64_i8 v[40:43], v[4:7], v[40:43], 0
	v_mfma_i32_16x16x64_i8 v[36:39], v[8:11], v[44:47], v[36:39]
	v_mfma_i32_16x16x64_i8 v[40:43], v[0:3], v[44:47], v[40:43]
	v_mfma_i32_16x16x64_i8 v[44:47], v[12:15], v[48:51], 0
	v_mfma_i32_16x16x64_i8 v[48:51], v[4:7], v[48:51], 0
	v_mfma_i32_16x16x64_i8 v[44:47], v[8:11], v[52:55], v[44:47]
	v_mfma_i32_16x16x64_i8 v[48:51], v[0:3], v[52:55], v[48:51]
	v_mfma_i32_16x16x64_i8 v[52:55], v[12:15], v[56:59], 0
	v_mfma_i32_16x16x64_i8 v[56:59], v[4:7], v[56:59], 0
	v_mfma_i32_16x16x64_i8 v[52:55], v[8:11], v[60:63], v[52:55]
	v_mfma_i32_16x16x64_i8 v[56:59], v[0:3], v[60:63], v[56:59]
	s_barrier
	ds_read_b128 v[60:63], v206 offset:16384
	ds_read_b128 v[100:103], v206 offset:17408
	ds_read_b128 v[104:107], v206 offset:18432
	ds_read_b128 v[108:111], v206 offset:19456
	ds_read_b128 v[112:115], v206 offset:20480
	ds_read_b128 v[116:119], v206 offset:21504
	ds_read_b128 v[120:123], v206 offset:22528
	ds_read_b128 v[124:127], v206 offset:23552
	s_add_i32 m0, s46, 0x10000
	s_nop 0
	global_load_lds_dwordx4 v200, s[62:63]
	s_nop 0
	s_add_i32 m0, s46, 0x12000
	s_nop 0
	global_load_lds_dwordx4 v202, s[62:63]
	s_add_u32 s62, s24, 0x40100
	s_addc_u32 s63, s25, 0
	s_add_i32 m0, s46, 0x14000
	s_nop 0
	global_load_lds_dwordx4 v200, s[62:63]
	s_nop 0
	s_add_i32 m0, s46, 0x16000
	s_nop 0
	global_load_lds_dwordx4 v202, s[62:63]
	s_nop 0
	s_add_i32 m0, s46, 0
	s_nop 0
	global_load_lds_dwordx4 v199, s[26:27]
	s_nop 0
	s_add_i32 m0, s46, 0x2000
	s_nop 0
	global_load_lds_dwordx4 v201, s[26:27]
	s_waitcnt vmcnt(16) lgkmcnt(0)
	s_barrier
	v_mfma_i32_16x16x64_i8 v[128:131], v[28:31], v[60:63], 0
	v_mfma_i32_16x16x64_i8 v[210:213], v[24:27], v[100:103], v[128:131]
	v_mfma_i32_16x16x64_i8 v[128:131], v[20:23], v[60:63], 0
	v_mfma_i32_16x16x64_i8 v[214:217], v[16:19], v[100:103], v[128:131]
	v_mfma_i32_16x16x64_i8 v[128:131], v[28:31], v[104:107], 0
	v_mfma_i32_16x16x64_i8 v[218:221], v[24:27], v[108:111], v[128:131]
	v_mfma_i32_16x16x64_i8 v[128:131], v[20:23], v[104:107], 0
	v_mfma_i32_16x16x64_i8 v[222:225], v[16:19], v[108:111], v[128:131]
	v_mfma_i32_16x16x64_i8 v[128:131], v[28:31], v[112:115], 0
	v_mfma_i32_16x16x64_i8 v[226:229], v[24:27], v[116:119], v[128:131]
	v_mfma_i32_16x16x64_i8 v[128:131], v[20:23], v[112:115], 0
	v_mfma_i32_16x16x64_i8 v[28:31], v[28:31], v[120:123], 0
	v_mfma_i32_16x16x64_i8 v[20:23], v[20:23], v[120:123], 0
	v_mfma_i32_16x16x64_i8 v[230:233], v[16:19], v[116:119], v[128:131]
	v_mfma_i32_16x16x64_i8 v[24:27], v[24:27], v[124:127], v[28:31]
	v_mfma_i32_16x16x64_i8 v[20:23], v[16:19], v[124:127], v[20:23]
	v_mfma_i32_16x16x64_i8 v[16:19], v[12:15], v[60:63], 0
	v_mfma_i32_16x16x64_i8 v[28:31], v[8:11], v[100:103], v[16:19]
	v_mfma_i32_16x16x64_i8 v[16:19], v[4:7], v[60:63], 0
	v_mfma_i32_16x16x64_i8 v[60:63], v[0:3], v[100:103], v[16:19]
	v_mfma_i32_16x16x64_i8 v[16:19], v[12:15], v[104:107], 0
	v_mfma_i32_16x16x64_i8 v[100:103], v[8:11], v[108:111], v[16:19]
	v_mfma_i32_16x16x64_i8 v[16:19], v[4:7], v[104:107], 0
	v_mfma_i32_16x16x64_i8 v[234:237], v[0:3], v[108:111], v[16:19]
	v_mfma_i32_16x16x64_i8 v[16:19], v[12:15], v[112:115], 0
	v_mfma_i32_16x16x64_i8 v[238:241], v[8:11], v[116:119], v[16:19]
	v_mfma_i32_16x16x64_i8 v[16:19], v[4:7], v[112:115], 0
	v_mfma_i32_16x16x64_i8 v[12:15], v[12:15], v[120:123], 0
	v_mfma_i32_16x16x64_i8 v[4:7], v[4:7], v[120:123], 0
	v_mfma_i32_16x16x64_i8 v[12:15], v[8:11], v[124:127], v[12:15]
	v_mfma_i32_16x16x64_i8 v[4:7], v[0:3], v[124:127], v[4:7]
	v_mfma_i32_16x16x64_i8 v[242:245], v[0:3], v[116:119], v[16:19]
	s_barrier
	ds_read_b128 v[0:3], v207
	ds_read_b128 v[8:11], v207 offset:1024
	ds_read_b128 v[108:111], v207 offset:2048
	ds_read_b128 v[116:119], v207 offset:3072
	ds_read_b128 v[246:249], v208
	ds_read_b128 v[250:253], v208 offset:1024
	ds_read_b128 v[192:195], v208 offset:2048
	ds_read_b128 v[64:67], v208 offset:3072
	ds_read_b128 v[16:19], v206 offset:32768
	ds_read_b128 v[104:107], v206 offset:33792
	ds_read_b128 v[112:115], v206 offset:34816
	ds_read_b128 v[120:123], v206 offset:35840
	ds_read_b128 v[124:127], v206 offset:36864
	ds_read_b128 v[140:143], v206 offset:37888
	ds_read_b128 v[68:71], v206 offset:38912
	ds_read_b128 v[72:75], v206 offset:39936
	s_add_u32 s28, s28, 0x40100
	s_addc_u32 s29, s29, 0
	s_add_i32 m0, s46, 0x4000
	s_nop 0
	global_load_lds_dwordx4 v199, s[28:29]
	s_nop 0
	s_add_i32 m0, s46, 0x6000
	s_nop 0
	global_load_lds_dwordx4 v201, s[28:29]
	s_waitcnt vmcnt(8) lgkmcnt(0)
	s_barrier
	v_mfma_i32_16x16x64_i8 v[76:79], v[108:111], v[112:115], v[76:79]
	v_mfma_i32_16x16x64_i8 v[128:131], v[0:3], v[16:19], v[132:135]
	v_mfma_i32_16x16x64_i8 v[160:163], v[116:119], v[120:123], v[76:79]
	v_mfma_i32_16x16x64_i8 v[76:79], v[0:3], v[124:127], v[80:83]
	v_mfma_i32_16x16x64_i8 v[184:187], v[8:11], v[104:107], v[128:131]
	v_mfma_i32_16x16x64_i8 v[128:131], v[108:111], v[16:19], v[136:139]
	v_mfma_i32_16x16x64_i8 v[152:155], v[8:11], v[140:143], v[76:79]
	v_mfma_i32_16x16x64_i8 v[76:79], v[108:111], v[124:127], v[84:87]
	v_mfma_i32_16x16x64_i8 v[176:179], v[116:119], v[104:107], v[128:131]
	v_mfma_i32_16x16x64_i8 v[128:131], v[0:3], v[112:115], v[144:147]
	v_mfma_i32_16x16x64_i8 v[144:147], v[116:119], v[140:143], v[76:79]
	v_mfma_i32_16x16x64_i8 v[76:79], v[0:3], v[68:71], v[88:91]
	v_mfma_i32_16x16x64_i8 v[136:139], v[8:11], v[72:75], v[76:79]
	v_mfma_i32_16x16x64_i8 v[76:79], v[108:111], v[68:71], v[92:95]
	v_mfma_i32_16x16x64_i8 v[168:171], v[8:11], v[120:123], v[128:131]
	v_mfma_i32_16x16x64_i8 v[128:131], v[116:119], v[72:75], v[76:79]
	v_mfma_i32_16x16x64_i8 v[76:79], v[246:249], v[16:19], v[96:99]
	v_mfma_i32_16x16x64_i8 v[16:19], v[192:195], v[16:19], v[32:35]
	v_mfma_i32_16x16x64_i8 v[180:183], v[64:67], v[104:107], v[16:19]
	v_mfma_i32_16x16x64_i8 v[16:19], v[246:249], v[112:115], v[36:39]
	v_mfma_i32_16x16x64_i8 v[172:175], v[250:253], v[120:123], v[16:19]
	v_mfma_i32_16x16x64_i8 v[16:19], v[192:195], v[112:115], v[40:43]
	v_mfma_i32_16x16x64_i8 v[164:167], v[64:67], v[120:123], v[16:19]
	v_mfma_i32_16x16x64_i8 v[16:19], v[246:249], v[124:127], v[44:47]
	v_mfma_i32_16x16x64_i8 v[156:159], v[250:253], v[140:143], v[16:19]
	v_mfma_i32_16x16x64_i8 v[16:19], v[192:195], v[124:127], v[48:51]
	v_mfma_i32_16x16x64_i8 v[148:151], v[64:67], v[140:143], v[16:19]
	v_mfma_i32_16x16x64_i8 v[16:19], v[246:249], v[68:71], v[52:55]
	v_mfma_i32_16x16x64_i8 v[140:143], v[250:253], v[72:75], v[16:19]
	v_mfma_i32_16x16x64_i8 v[16:19], v[192:195], v[68:71], v[56:59]
	v_mfma_i32_16x16x64_i8 v[188:191], v[250:253], v[104:107], v[76:79]
	v_mfma_i32_16x16x64_i8 v[132:135], v[64:67], v[72:75], v[16:19]
	s_barrier
	ds_read_b128 v[32:35], v206 offset:49152
	ds_read_b128 v[36:39], v206 offset:50176
	ds_read_b128 v[40:43], v206 offset:51200
	ds_read_b128 v[44:47], v206 offset:52224
	ds_read_b128 v[52:55], v206 offset:53248
	ds_read_b128 v[56:59], v206 offset:54272
	ds_read_b128 v[68:71], v206 offset:55296
	ds_read_b128 v[72:75], v206 offset:56320
	s_add_i32 m0, s46, 0x18000
	s_nop 0
	global_load_lds_dwordx4 v200, s[36:37]
	s_nop 0
	s_add_i32 m0, s46, 0x1a000
	s_nop 0
	global_load_lds_dwordx4 v202, s[36:37]
	s_add_u32 s28, s24, 0x40180
	s_addc_u32 s29, s25, 0
	s_add_i32 m0, s46, 0x1c000
	s_nop 0
	global_load_lds_dwordx4 v200, s[28:29]
	s_nop 0
	s_add_i32 m0, s46, 0x1e000
	s_nop 0
	global_load_lds_dwordx4 v202, s[28:29]
	s_nop 0
	s_add_i32 m0, s46, 0x8000
	s_nop 0
	global_load_lds_dwordx4 v199, s[34:35]
	s_nop 0
	s_add_i32 m0, s46, 0xa000
	s_nop 0
	global_load_lds_dwordx4 v201, s[34:35]
	s_waitcnt vmcnt(8) lgkmcnt(0)
	s_barrier
	v_mfma_i32_16x16x64_i8 v[16:19], v[0:3], v[32:35], v[210:213]
	v_mfma_i32_16x16x64_i8 v[120:123], v[8:11], v[36:39], v[16:19]
	v_mfma_i32_16x16x64_i8 v[16:19], v[108:111], v[32:35], v[214:217]
	v_mfma_i32_16x16x64_i8 v[112:115], v[116:119], v[36:39], v[16:19]
	v_mfma_i32_16x16x64_i8 v[16:19], v[0:3], v[40:43], v[218:221]
	v_mfma_i32_16x16x64_i8 v[104:107], v[8:11], v[44:47], v[16:19]
	v_mfma_i32_16x16x64_i8 v[16:19], v[108:111], v[40:43], v[222:225]
	v_mfma_i32_16x16x64_i8 v[96:99], v[116:119], v[44:47], v[16:19]
	v_mfma_i32_16x16x64_i8 v[16:19], v[0:3], v[52:55], v[226:229]
	v_mfma_i32_16x16x64_i8 v[0:3], v[0:3], v[68:71], v[24:27]
	v_mfma_i32_16x16x64_i8 v[48:51], v[8:11], v[56:59], v[16:19]
	v_mfma_i32_16x16x64_i8 v[16:19], v[108:111], v[52:55], v[230:233]
	v_mfma_i32_16x16x64_i8 v[8:11], v[8:11], v[72:75], v[0:3]
	v_mfma_i32_16x16x64_i8 v[0:3], v[108:111], v[68:71], v[20:23]
	v_mfma_i32_16x16x64_i8 v[16:19], v[116:119], v[56:59], v[16:19]
	v_mfma_i32_16x16x64_i8 v[0:3], v[116:119], v[72:75], v[0:3]
	v_mfma_i32_16x16x64_i8 v[20:23], v[246:249], v[32:35], v[28:31]
	v_mfma_i32_16x16x64_i8 v[124:127], v[250:253], v[36:39], v[20:23]
	v_mfma_i32_16x16x64_i8 v[20:23], v[192:195], v[32:35], v[60:63]
	v_mfma_i32_16x16x64_i8 v[116:119], v[64:67], v[36:39], v[20:23]
	v_mfma_i32_16x16x64_i8 v[20:23], v[246:249], v[40:43], v[100:103]
	v_mfma_i32_16x16x64_i8 v[108:111], v[250:253], v[44:47], v[20:23]
	v_mfma_i32_16x16x64_i8 v[20:23], v[192:195], v[40:43], v[234:237]
	v_mfma_i32_16x16x64_i8 v[100:103], v[64:67], v[44:47], v[20:23]
	v_mfma_i32_16x16x64_i8 v[20:23], v[246:249], v[52:55], v[238:241]
	v_mfma_i32_16x16x64_i8 v[60:63], v[250:253], v[56:59], v[20:23]
	v_mfma_i32_16x16x64_i8 v[20:23], v[192:195], v[52:55], v[242:245]
	v_mfma_i32_16x16x64_i8 v[12:15], v[246:249], v[68:71], v[12:15]
	v_mfma_i32_16x16x64_i8 v[4:7], v[192:195], v[68:71], v[4:7]
	v_mfma_i32_16x16x64_i8 v[44:47], v[64:67], v[56:59], v[20:23]
	v_mfma_i32_16x16x64_i8 v[12:15], v[250:253], v[72:75], v[12:15]
	v_mfma_i32_16x16x64_i8 v[4:7], v[64:67], v[72:75], v[4:7]
	s_barrier
	s_add_u32 s28, s44, s30
	s_addc_u32 s29, s45, s31
	s_add_u32 s61, s24, 0x200
	s_addc_u32 s62, s25, 0
	s_add_i32 s63, s38, 0
	s_add_i32 s63, s63, 0x20000

.LBB0_1410:
	ds_read_b128 v[0:3], v138
	ds_read_b128 v[4:7], v138 offset:1024
	ds_read_b128 v[8:11], v138 offset:2048
	ds_read_b128 v[12:15], v138 offset:3072
	ds_read_b128 v[16:19], v139
	ds_read_b128 v[20:23], v139 offset:1024
	ds_read_b128 v[24:27], v139 offset:2048
	ds_read_b128 v[28:31], v139 offset:3072
	ds_read_b128 v[32:35], v140
	ds_read_b128 v[36:39], v140 offset:1024
	ds_read_b128 v[40:43], v140 offset:2048
	ds_read_b128 v[44:47], v140 offset:3072
	ds_read_b128 v[48:51], v140 offset:4096
	ds_read_b128 v[52:55], v140 offset:5120
	ds_read_b128 v[56:59], v140 offset:6144
	ds_read_b128 v[60:63], v140 offset:7168
	s_lshl_b64 s[20:21], s[16:17], 19
	s_add_u32 s20, s39, s20
	s_addc_u32 s21, s40, s21
	s_and_b64 s[6:7], exec, s[6:7]
	s_cselect_b32 s2, s21, s29
	s_cselect_b32 s15, s20, s28
	s_add_u32 s6, s28, 0x100
	s_addc_u32 s7, s29, 0
	s_add_u32 s36, s26, 0x100
	s_addc_u32 s37, s27, 0
	s_add_u32 s30, s28, 0x180
	s_addc_u32 s31, s29, 0
	s_add_u32 s34, s26, 0x180
	s_addc_u32 s35, s27, 0
	s_add_u32 s54, s28, 0x40080
	s_addc_u32 s55, s29, 0
	s_add_i32 m0, s47, 0xc000
	s_nop 0
	global_load_lds_dwordx4 v134, s[54:55]
	s_nop 0
	s_add_i32 m0, s47, 0xe000
	s_nop 0
	global_load_lds_dwordx4 v136, s[54:55]
	s_waitcnt vmcnt(16) lgkmcnt(0)
	s_barrier
	v_mfma_f32_16x16x128_f8f6f4 v[64:67], v[0:7], v[32:39], 0
	v_mfma_f32_16x16x128_f8f6f4 v[68:71], v[8:15], v[32:39], 0
	v_mfma_f32_16x16x128_f8f6f4 v[76:79], v[8:15], v[40:47], 0
	v_mfma_f32_16x16x128_f8f6f4 v[72:75], v[0:7], v[40:47], 0
	v_mfma_f32_16x16x128_f8f6f4 v[80:83], v[0:7], v[48:55], 0
	v_mfma_f32_16x16x128_f8f6f4 v[88:91], v[8:15], v[48:55], 0
	v_mfma_f32_16x16x128_f8f6f4 v[104:107], v[8:15], v[56:63], 0
	v_mfma_f32_16x16x128_f8f6f4 v[92:95], v[0:7], v[56:63], 0
	v_mfma_f32_16x16x128_f8f6f4 v[108:111], v[16:23], v[32:39], 0
	v_mfma_f32_16x16x128_f8f6f4 v[124:127], v[24:31], v[32:39], 0
	v_mfma_f32_16x16x128_f8f6f4 v[166:169], v[24:31], v[40:47], 0
	v_mfma_f32_16x16x128_f8f6f4 v[162:165], v[16:23], v[40:47], 0
	v_mfma_f32_16x16x128_f8f6f4 v[170:173], v[16:23], v[48:55], 0
	v_mfma_f32_16x16x128_f8f6f4 v[174:177], v[24:31], v[48:55], 0
	v_mfma_f32_16x16x128_f8f6f4 v[182:185], v[24:31], v[56:63], 0
	v_mfma_f32_16x16x128_f8f6f4 v[178:181], v[16:23], v[56:63], 0
	s_barrier
	ds_read_b128 v[32:35], v140 offset:16384
	ds_read_b128 v[36:39], v140 offset:17408
	ds_read_b128 v[40:43], v140 offset:18432
	ds_read_b128 v[44:47], v140 offset:19456
	ds_read_b128 v[48:51], v140 offset:20480
	ds_read_b128 v[52:55], v140 offset:21504
	ds_read_b128 v[56:59], v140 offset:22528
	ds_read_b128 v[60:63], v140 offset:23552
	s_add_i32 m0, s47, 0x10000
	s_nop 0
	global_load_lds_dwordx4 v135, s[36:37]
	s_nop 0
	s_add_i32 m0, s47, 0x12000
	s_nop 0
	global_load_lds_dwordx4 v137, s[36:37]
	s_add_u32 s36, s26, 0x40100
	s_addc_u32 s37, s27, 0
	s_add_i32 m0, s47, 0x14000
	s_nop 0
	global_load_lds_dwordx4 v135, s[36:37]
	s_nop 0
	s_add_i32 m0, s47, 0x16000
	s_nop 0
	global_load_lds_dwordx4 v137, s[36:37]
	s_nop 0
	s_add_i32 m0, s47, 0
	s_nop 0
	global_load_lds_dwordx4 v134, s[6:7]
	s_nop 0
	s_add_i32 m0, s47, 0x2000
	s_nop 0
	global_load_lds_dwordx4 v136, s[6:7]
	s_waitcnt vmcnt(16) lgkmcnt(0)
	s_barrier
	v_mfma_f32_16x16x128_f8f6f4 v[186:189], v[0:7], v[32:39], 0
	v_mfma_f32_16x16x128_f8f6f4 v[190:193], v[8:15], v[32:39], 0
	v_mfma_f32_16x16x128_f8f6f4 v[198:201], v[8:15], v[40:47], 0
	v_mfma_f32_16x16x128_f8f6f4 v[194:197], v[0:7], v[40:47], 0
	v_mfma_f32_16x16x128_f8f6f4 v[202:205], v[0:7], v[48:55], 0
	v_mfma_f32_16x16x128_f8f6f4 v[206:209], v[8:15], v[48:55], 0
	v_mfma_f32_16x16x128_f8f6f4 v[214:217], v[8:15], v[56:63], 0
	v_mfma_f32_16x16x128_f8f6f4 v[210:213], v[0:7], v[56:63], 0
	v_mfma_f32_16x16x128_f8f6f4 v[218:221], v[16:23], v[32:39], 0
	v_mfma_f32_16x16x128_f8f6f4 v[222:225], v[24:31], v[32:39], 0
	v_mfma_f32_16x16x128_f8f6f4 v[230:233], v[24:31], v[40:47], 0
	v_mfma_f32_16x16x128_f8f6f4 v[226:229], v[16:23], v[40:47], 0
	v_mfma_f32_16x16x128_f8f6f4 v[234:237], v[16:23], v[48:55], 0
	v_mfma_f32_16x16x128_f8f6f4 v[238:241], v[24:31], v[48:55], 0
	v_mfma_f32_16x16x128_f8f6f4 v[246:249], v[24:31], v[56:63], 0
	v_mfma_f32_16x16x128_f8f6f4 v[242:245], v[16:23], v[56:63], 0
	s_barrier
	ds_read_b128 v[0:3], v141
	ds_read_b128 v[4:7], v141 offset:1024
	ds_read_b128 v[8:11], v141 offset:2048
	ds_read_b128 v[12:15], v141 offset:3072
	ds_read_b128 v[146:149], v142
	ds_read_b128 v[150:153], v142 offset:1024
	ds_read_b128 v[154:157], v142 offset:2048
	ds_read_b128 v[158:161], v142 offset:3072
	ds_read_b128 v[16:19], v140 offset:32768
	ds_read_b128 v[20:23], v140 offset:33792
	ds_read_b128 v[24:27], v140 offset:34816
	ds_read_b128 v[28:31], v140 offset:35840
	ds_read_b128 v[32:35], v140 offset:36864
	ds_read_b128 v[36:39], v140 offset:37888
	ds_read_b128 v[40:43], v140 offset:38912
	ds_read_b128 v[44:47], v140 offset:39936
	s_add_u32 s28, s28, 0x40100
	s_addc_u32 s29, s29, 0
	s_add_i32 m0, s47, 0x4000
	s_nop 0
	global_load_lds_dwordx4 v134, s[28:29]
	s_nop 0
	s_add_i32 m0, s47, 0x6000
	s_nop 0
	global_load_lds_dwordx4 v136, s[28:29]
	s_waitcnt vmcnt(8) lgkmcnt(0)
	s_barrier
	v_mfma_f32_16x16x128_f8f6f4 v[112:115], v[0:7], v[16:23], v[64:67]
	v_mfma_f32_16x16x128_f8f6f4 v[116:119], v[8:15], v[16:23], v[68:71]
	v_mfma_f32_16x16x128_f8f6f4 v[100:103], v[0:7], v[24:31], v[72:75]
	v_mfma_f32_16x16x128_f8f6f4 v[96:99], v[8:15], v[24:31], v[76:79]
	v_mfma_f32_16x16x128_f8f6f4 v[84:87], v[0:7], v[32:39], v[80:83]
	v_mfma_f32_16x16x128_f8f6f4 v[80:83], v[8:15], v[32:39], v[88:91]
	v_mfma_f32_16x16x128_f8f6f4 v[60:63], v[0:7], v[40:47], v[92:95]
	v_mfma_f32_16x16x128_f8f6f4 v[56:59], v[8:15], v[40:47], v[104:107]
	v_mfma_f32_16x16x128_f8f6f4 v[120:123], v[146:153], v[16:23], v[108:111]
	v_mfma_f32_16x16x128_f8f6f4 v[124:127], v[154:161], v[16:23], v[124:127]
	v_mfma_f32_16x16x128_f8f6f4 v[108:111], v[146:153], v[24:31], v[162:165]
	v_mfma_f32_16x16x128_f8f6f4 v[104:107], v[154:161], v[24:31], v[166:169]
	v_mfma_f32_16x16x128_f8f6f4 v[92:95], v[146:153], v[32:39], v[170:173]
	v_mfma_f32_16x16x128_f8f6f4 v[88:91], v[154:161], v[32:39], v[174:177]
	v_mfma_f32_16x16x128_f8f6f4 v[76:79], v[146:153], v[40:47], v[178:181]
	v_mfma_f32_16x16x128_f8f6f4 v[72:75], v[154:161], v[40:47], v[182:185]
	s_barrier
	ds_read_b128 v[24:27], v140 offset:49152
	ds_read_b128 v[28:31], v140 offset:50176
	ds_read_b128 v[162:165], v140 offset:51200
	ds_read_b128 v[166:169], v140 offset:52224
	ds_read_b128 v[170:173], v140 offset:53248
	ds_read_b128 v[174:177], v140 offset:54272
	ds_read_b128 v[178:181], v140 offset:55296
	ds_read_b128 v[182:185], v140 offset:56320
	s_add_i32 m0, s47, 0x18000
	s_nop 0
	global_load_lds_dwordx4 v135, s[34:35]
	s_nop 0
	s_add_i32 m0, s47, 0x1a000
	s_nop 0
	global_load_lds_dwordx4 v137, s[34:35]
	s_add_u32 s28, s26, 0x40180
	s_addc_u32 s29, s27, 0
	s_add_i32 m0, s47, 0x1c000
	s_nop 0
	global_load_lds_dwordx4 v135, s[28:29]
	s_nop 0
	s_add_i32 m0, s47, 0x1e000
	s_nop 0
	global_load_lds_dwordx4 v137, s[28:29]
	s_nop 0
	s_add_i32 m0, s47, 0x8000
	s_nop 0
	global_load_lds_dwordx4 v134, s[30:31]
	s_nop 0
	s_add_i32 m0, s47, 0xa000
	s_nop 0
	global_load_lds_dwordx4 v136, s[30:31]
	s_waitcnt vmcnt(8) lgkmcnt(0)
	s_barrier
	v_mfma_f32_16x16x128_f8f6f4 v[52:55], v[0:7], v[24:31], v[186:189]
	v_mfma_f32_16x16x128_f8f6f4 v[48:51], v[8:15], v[24:31], v[190:193]
	v_mfma_f32_16x16x128_f8f6f4 v[36:39], v[0:7], v[162:169], v[194:197]
	v_mfma_f32_16x16x128_f8f6f4 v[32:35], v[8:15], v[162:169], v[198:201]
	v_mfma_f32_16x16x128_f8f6f4 v[20:23], v[0:7], v[170:177], v[202:205]
	v_mfma_f32_16x16x128_f8f6f4 v[16:19], v[8:15], v[170:177], v[206:209]
	v_mfma_f32_16x16x128_f8f6f4 v[4:7], v[0:7], v[178:185], v[210:213]
	v_mfma_f32_16x16x128_f8f6f4 v[0:3], v[8:15], v[178:185], v[214:217]
	v_mfma_f32_16x16x128_f8f6f4 v[68:71], v[146:153], v[24:31], v[218:221]
	v_mfma_f32_16x16x128_f8f6f4 v[64:67], v[154:161], v[24:31], v[222:225]
	v_mfma_f32_16x16x128_f8f6f4 v[44:47], v[146:153], v[162:169], v[226:229]
	v_mfma_f32_16x16x128_f8f6f4 v[40:43], v[154:161], v[162:169], v[230:233]
	v_mfma_f32_16x16x128_f8f6f4 v[28:31], v[146:153], v[170:177], v[234:237]
	v_mfma_f32_16x16x128_f8f6f4 v[24:27], v[154:161], v[170:177], v[238:241]
	v_mfma_f32_16x16x128_f8f6f4 v[12:15], v[146:153], v[178:185], v[242:245]
	v_mfma_f32_16x16x128_f8f6f4 v[8:11], v[154:161], v[178:185], v[246:249]
	s_barrier
	s_add_u32 s17, s26, 0x200
	s_addc_u32 s54, s27, 0
	s_mov_b32 s55, 0
